# adaLN GEMV K-loop in MOD phase: the 8 weight loads of an unrolled trip issued together instead of load-wait-fma per step
# baseline (speedup 1.0000x reference)
.LBB0_32:
	s_mov_b32 s98, 0xfffe8000
	s_mov_b32 s99, -1
	v_lshl_add_u64 v[104:105], v[40:41], 0, s[98:99]
	global_load_dwordx4 v[72:75], v[104:105], off
	s_mov_b32 s98, 0xfffee000
	s_mov_b32 s99, -1
	v_lshl_add_u64 v[104:105], v[40:41], 0, s[98:99]
	global_load_dwordx4 v[76:79], v[104:105], off
	s_mov_b32 s98, 0xffff4000
	s_mov_b32 s99, -1
	v_lshl_add_u64 v[104:105], v[40:41], 0, s[98:99]
	global_load_dwordx4 v[80:83], v[104:105], off
	s_mov_b32 s98, 0xffffa000
	s_mov_b32 s99, -1
	v_lshl_add_u64 v[104:105], v[40:41], 0, s[98:99]
	global_load_dwordx4 v[84:87], v[104:105], off
	global_load_dwordx4 v[88:91], v[40:41], off
	s_mov_b32 s98, 0x6000
	s_mov_b32 s99, 0
	v_lshl_add_u64 v[104:105], v[40:41], 0, s[98:99]
	global_load_dwordx4 v[92:95], v[104:105], off
	s_mov_b32 s98, 0xc000
	s_mov_b32 s99, 0
	v_lshl_add_u64 v[104:105], v[40:41], 0, s[98:99]
	global_load_dwordx4 v[96:99], v[104:105], off
	s_mov_b32 s98, 0x12000
	s_mov_b32 s99, 0
	v_lshl_add_u64 v[104:105], v[40:41], 0, s[98:99]
	global_load_dwordx4 v[100:103], v[104:105], off
	v_add_u32_e32 v63, -2, v49
	s_nop 0
	ds_read2st64_b32 v[54:55], v48 offset1:16
	ds_read2st64_b32 v[56:57], v48 offset0:32 offset1:48
	ds_read2st64_b32 v[58:59], v48 offset0:64 offset1:80
	ds_read2st64_b32 v[60:61], v48 offset0:96 offset1:112
	ds_read_b32 v62, v48 offset:32768
	s_waitcnt lgkmcnt(0)
	v_mov_b32_e32 v64, v55
	v_mov_b32_e32 v66, v57
	v_mov_b32_e32 v68, v59
	v_mov_b32_e32 v70, v61
	v_cmp_lt_i32_e32 vcc, v63, v43
	s_or_b64 s[20:21], s[20:21], exec
	s_waitcnt vmcnt(7)
	v_pk_fma_f32 v[34:35], v[74:75], v[54:55], v[34:35] op_sel_hi:[1,0,1]
	v_pk_fma_f32 v[32:33], v[72:73], v[54:55], v[32:33] op_sel_hi:[1,0,1]
	v_pk_fma_f32 v[30:31], v[74:75], v[64:65], v[30:31] op_sel_hi:[1,0,1]
	v_pk_fma_f32 v[28:29], v[72:73], v[64:65], v[28:29] op_sel_hi:[1,0,1]
	v_pk_fma_f32 v[26:27], v[74:75], v[56:57], v[26:27] op_sel_hi:[1,0,1]
	v_pk_fma_f32 v[24:25], v[72:73], v[56:57], v[24:25] op_sel_hi:[1,0,1]
	v_pk_fma_f32 v[22:23], v[74:75], v[66:67], v[22:23] op_sel_hi:[1,0,1]
	v_pk_fma_f32 v[20:21], v[72:73], v[66:67], v[20:21] op_sel_hi:[1,0,1]
	v_pk_fma_f32 v[18:19], v[74:75], v[58:59], v[18:19] op_sel_hi:[1,0,1]
	v_pk_fma_f32 v[16:17], v[72:73], v[58:59], v[16:17] op_sel_hi:[1,0,1]
	v_pk_fma_f32 v[14:15], v[74:75], v[68:69], v[14:15] op_sel_hi:[1,0,1]
	v_pk_fma_f32 v[12:13], v[72:73], v[68:69], v[12:13] op_sel_hi:[1,0,1]
	v_pk_fma_f32 v[10:11], v[74:75], v[60:61], v[10:11] op_sel_hi:[1,0,1]
	v_pk_fma_f32 v[8:9], v[72:73], v[60:61], v[8:9] op_sel_hi:[1,0,1]
	v_pk_fma_f32 v[6:7], v[74:75], v[70:71], v[6:7] op_sel_hi:[1,0,1]
	v_pk_fma_f32 v[4:5], v[72:73], v[70:71], v[4:5] op_sel_hi:[1,0,1]
	v_pk_fma_f32 v[2:3], v[74:75], v[62:63], v[2:3] op_sel_hi:[1,0,1]
	v_pk_fma_f32 v[0:1], v[72:73], v[62:63], v[0:1] op_sel_hi:[1,0,1]
	s_and_saveexec_b64 s[22:23], vcc
	s_cbranch_execz .LBB0_31
	v_add_u32_e32 v62, 4, v48
	s_nop 0
	ds_read_b32 v54, v48 offset:32772
	ds_read2st64_b32 v[56:57], v62 offset1:16
	ds_read2st64_b32 v[58:59], v62 offset0:32 offset1:48
	ds_read2st64_b32 v[60:61], v62 offset0:64 offset1:80
	ds_read2st64_b32 v[62:63], v62 offset0:96 offset1:112
	v_add_u32_e32 v55, -1, v49
	s_waitcnt lgkmcnt(3)
	v_mov_b32_e32 v64, v57
	s_waitcnt lgkmcnt(2)
	v_mov_b32_e32 v66, v59
	s_waitcnt lgkmcnt(1)
	v_mov_b32_e32 v68, v61
	s_waitcnt lgkmcnt(0)
	v_mov_b32_e32 v70, v63
	v_cmp_lt_i32_e32 vcc, v55, v43
	s_mov_b64 s[34:35], -1
	s_waitcnt vmcnt(6)
	v_pk_fma_f32 v[34:35], v[78:79], v[56:57], v[34:35] op_sel_hi:[1,0,1]
	v_pk_fma_f32 v[32:33], v[76:77], v[56:57], v[32:33] op_sel_hi:[1,0,1]
	v_pk_fma_f32 v[30:31], v[78:79], v[64:65], v[30:31] op_sel_hi:[1,0,1]
	v_pk_fma_f32 v[28:29], v[76:77], v[64:65], v[28:29] op_sel_hi:[1,0,1]
	v_pk_fma_f32 v[26:27], v[78:79], v[58:59], v[26:27] op_sel_hi:[1,0,1]
	v_pk_fma_f32 v[24:25], v[76:77], v[58:59], v[24:25] op_sel_hi:[1,0,1]
	v_pk_fma_f32 v[22:23], v[78:79], v[66:67], v[22:23] op_sel_hi:[1,0,1]
	v_pk_fma_f32 v[20:21], v[76:77], v[66:67], v[20:21] op_sel_hi:[1,0,1]
	v_pk_fma_f32 v[18:19], v[78:79], v[60:61], v[18:19] op_sel_hi:[1,0,1]
	v_pk_fma_f32 v[16:17], v[76:77], v[60:61], v[16:17] op_sel_hi:[1,0,1]
	v_pk_fma_f32 v[14:15], v[78:79], v[68:69], v[14:15] op_sel_hi:[1,0,1]
	v_pk_fma_f32 v[12:13], v[76:77], v[68:69], v[12:13] op_sel_hi:[1,0,1]
	v_pk_fma_f32 v[10:11], v[78:79], v[62:63], v[10:11] op_sel_hi:[1,0,1]
	v_pk_fma_f32 v[8:9], v[76:77], v[62:63], v[8:9] op_sel_hi:[1,0,1]
	v_pk_fma_f32 v[6:7], v[78:79], v[70:71], v[6:7] op_sel_hi:[1,0,1]
	v_pk_fma_f32 v[4:5], v[76:77], v[70:71], v[4:5] op_sel_hi:[1,0,1]
	v_pk_fma_f32 v[2:3], v[78:79], v[54:55], v[2:3] op_sel_hi:[1,0,1]
	v_pk_fma_f32 v[0:1], v[76:77], v[54:55], v[0:1] op_sel_hi:[1,0,1]
	s_and_saveexec_b64 s[0:1], vcc
	s_cbranch_execz .LBB0_30
	v_add_u32_e32 v55, 8, v48
	s_nop 0
	ds_read_b32 v54, v48 offset:32776
	ds_read2st64_b32 v[56:57], v55 offset1:16
	ds_read2st64_b32 v[58:59], v55 offset0:32 offset1:48
	ds_read2st64_b32 v[60:61], v55 offset0:64 offset1:80
	ds_read2st64_b32 v[62:63], v55 offset0:96 offset1:112
	v_cmp_lt_i32_e32 vcc, v49, v43
	s_waitcnt lgkmcnt(3)
	v_mov_b32_e32 v64, v57
	s_waitcnt lgkmcnt(2)
	v_mov_b32_e32 v66, v59
	s_waitcnt lgkmcnt(1)
	v_mov_b32_e32 v68, v61
	s_waitcnt lgkmcnt(0)
	v_mov_b32_e32 v70, v63
	s_mov_b64 s[36:37], -1
	s_waitcnt vmcnt(5)
	v_pk_fma_f32 v[34:35], v[82:83], v[56:57], v[34:35] op_sel_hi:[1,0,1]
	v_pk_fma_f32 v[32:33], v[80:81], v[56:57], v[32:33] op_sel_hi:[1,0,1]
	v_pk_fma_f32 v[30:31], v[82:83], v[64:65], v[30:31] op_sel_hi:[1,0,1]
	v_pk_fma_f32 v[28:29], v[80:81], v[64:65], v[28:29] op_sel_hi:[1,0,1]
	v_pk_fma_f32 v[26:27], v[82:83], v[58:59], v[26:27] op_sel_hi:[1,0,1]
	v_pk_fma_f32 v[24:25], v[80:81], v[58:59], v[24:25] op_sel_hi:[1,0,1]
	v_pk_fma_f32 v[22:23], v[82:83], v[66:67], v[22:23] op_sel_hi:[1,0,1]
	v_pk_fma_f32 v[20:21], v[80:81], v[66:67], v[20:21] op_sel_hi:[1,0,1]
	v_pk_fma_f32 v[18:19], v[82:83], v[60:61], v[18:19] op_sel_hi:[1,0,1]
	v_pk_fma_f32 v[16:17], v[80:81], v[60:61], v[16:17] op_sel_hi:[1,0,1]
	v_pk_fma_f32 v[14:15], v[82:83], v[68:69], v[14:15] op_sel_hi:[1,0,1]
	v_pk_fma_f32 v[12:13], v[80:81], v[68:69], v[12:13] op_sel_hi:[1,0,1]
	v_pk_fma_f32 v[10:11], v[82:83], v[62:63], v[10:11] op_sel_hi:[1,0,1]
	v_pk_fma_f32 v[8:9], v[80:81], v[62:63], v[8:9] op_sel_hi:[1,0,1]
	v_pk_fma_f32 v[6:7], v[82:83], v[70:71], v[6:7] op_sel_hi:[1,0,1]
	v_pk_fma_f32 v[4:5], v[80:81], v[70:71], v[4:5] op_sel_hi:[1,0,1]
	v_pk_fma_f32 v[2:3], v[82:83], v[54:55], v[2:3] op_sel_hi:[1,0,1]
	v_pk_fma_f32 v[0:1], v[80:81], v[54:55], v[0:1] op_sel_hi:[1,0,1]
	s_and_saveexec_b64 s[34:35], vcc
	s_cbranch_execz .LBB0_29
	v_add_u32_e32 v62, 12, v48
	s_nop 0
	ds_read_b32 v54, v48 offset:32780
	ds_read2st64_b32 v[56:57], v62 offset1:16
	ds_read2st64_b32 v[58:59], v62 offset0:32 offset1:48
	ds_read2st64_b32 v[60:61], v62 offset0:64 offset1:80
	ds_read2st64_b32 v[62:63], v62 offset0:96 offset1:112
	v_add_u32_e32 v55, 1, v49
	s_waitcnt lgkmcnt(3)
	v_mov_b32_e32 v64, v57
	s_waitcnt lgkmcnt(2)
	v_mov_b32_e32 v66, v59
	s_waitcnt lgkmcnt(1)
	v_mov_b32_e32 v68, v61
	s_waitcnt lgkmcnt(0)
	v_mov_b32_e32 v70, v63
	v_cmp_lt_i32_e32 vcc, v55, v43
	s_mov_b64 s[38:39], -1
	s_waitcnt vmcnt(4)
	v_pk_fma_f32 v[34:35], v[86:87], v[56:57], v[34:35] op_sel_hi:[1,0,1]
	v_pk_fma_f32 v[32:33], v[84:85], v[56:57], v[32:33] op_sel_hi:[1,0,1]
	v_pk_fma_f32 v[30:31], v[86:87], v[64:65], v[30:31] op_sel_hi:[1,0,1]
	v_pk_fma_f32 v[28:29], v[84:85], v[64:65], v[28:29] op_sel_hi:[1,0,1]
	v_pk_fma_f32 v[26:27], v[86:87], v[58:59], v[26:27] op_sel_hi:[1,0,1]
	v_pk_fma_f32 v[24:25], v[84:85], v[58:59], v[24:25] op_sel_hi:[1,0,1]
	v_pk_fma_f32 v[22:23], v[86:87], v[66:67], v[22:23] op_sel_hi:[1,0,1]
	v_pk_fma_f32 v[20:21], v[84:85], v[66:67], v[20:21] op_sel_hi:[1,0,1]
	v_pk_fma_f32 v[18:19], v[86:87], v[60:61], v[18:19] op_sel_hi:[1,0,1]
	v_pk_fma_f32 v[16:17], v[84:85], v[60:61], v[16:17] op_sel_hi:[1,0,1]
	v_pk_fma_f32 v[14:15], v[86:87], v[68:69], v[14:15] op_sel_hi:[1,0,1]
	v_pk_fma_f32 v[12:13], v[84:85], v[68:69], v[12:13] op_sel_hi:[1,0,1]
	v_pk_fma_f32 v[10:11], v[86:87], v[62:63], v[10:11] op_sel_hi:[1,0,1]
	v_pk_fma_f32 v[8:9], v[84:85], v[62:63], v[8:9] op_sel_hi:[1,0,1]
	v_pk_fma_f32 v[6:7], v[86:87], v[70:71], v[6:7] op_sel_hi:[1,0,1]
	v_pk_fma_f32 v[4:5], v[84:85], v[70:71], v[4:5] op_sel_hi:[1,0,1]
	v_pk_fma_f32 v[2:3], v[86:87], v[54:55], v[2:3] op_sel_hi:[1,0,1]
	v_pk_fma_f32 v[0:1], v[84:85], v[54:55], v[0:1] op_sel_hi:[1,0,1]
	s_and_saveexec_b64 s[36:37], vcc
	s_cbranch_execz .LBB0_28
	v_add_u32_e32 v62, 16, v48
	ds_read_b32 v54, v48 offset:32784
	ds_read2st64_b32 v[56:57], v62 offset1:16
	ds_read2st64_b32 v[58:59], v62 offset0:32 offset1:48
	ds_read2st64_b32 v[60:61], v62 offset0:64 offset1:80
	ds_read2st64_b32 v[62:63], v62 offset0:96 offset1:112
	v_add_u32_e32 v55, 2, v49
	s_waitcnt lgkmcnt(3)
	v_mov_b32_e32 v64, v57
	s_waitcnt lgkmcnt(2)
	v_mov_b32_e32 v66, v59
	s_waitcnt lgkmcnt(1)
	v_mov_b32_e32 v68, v61
	s_waitcnt lgkmcnt(0)
	v_mov_b32_e32 v70, v63
	v_cmp_lt_i32_e32 vcc, v55, v43
	s_mov_b64 s[40:41], -1
	s_waitcnt vmcnt(3)
	v_pk_fma_f32 v[34:35], v[90:91], v[56:57], v[34:35] op_sel_hi:[1,0,1]
	v_pk_fma_f32 v[32:33], v[88:89], v[56:57], v[32:33] op_sel_hi:[1,0,1]
	v_pk_fma_f32 v[30:31], v[90:91], v[64:65], v[30:31] op_sel_hi:[1,0,1]
	v_pk_fma_f32 v[28:29], v[88:89], v[64:65], v[28:29] op_sel_hi:[1,0,1]
	v_pk_fma_f32 v[26:27], v[90:91], v[58:59], v[26:27] op_sel_hi:[1,0,1]
	v_pk_fma_f32 v[24:25], v[88:89], v[58:59], v[24:25] op_sel_hi:[1,0,1]
	v_pk_fma_f32 v[22:23], v[90:91], v[66:67], v[22:23] op_sel_hi:[1,0,1]
	v_pk_fma_f32 v[20:21], v[88:89], v[66:67], v[20:21] op_sel_hi:[1,0,1]
	v_pk_fma_f32 v[18:19], v[90:91], v[60:61], v[18:19] op_sel_hi:[1,0,1]
	v_pk_fma_f32 v[16:17], v[88:89], v[60:61], v[16:17] op_sel_hi:[1,0,1]
	v_pk_fma_f32 v[14:15], v[90:91], v[68:69], v[14:15] op_sel_hi:[1,0,1]
	v_pk_fma_f32 v[12:13], v[88:89], v[68:69], v[12:13] op_sel_hi:[1,0,1]
	v_pk_fma_f32 v[10:11], v[90:91], v[62:63], v[10:11] op_sel_hi:[1,0,1]
	v_pk_fma_f32 v[8:9], v[88:89], v[62:63], v[8:9] op_sel_hi:[1,0,1]
	v_pk_fma_f32 v[6:7], v[90:91], v[70:71], v[6:7] op_sel_hi:[1,0,1]
	v_pk_fma_f32 v[4:5], v[88:89], v[70:71], v[4:5] op_sel_hi:[1,0,1]
	v_pk_fma_f32 v[2:3], v[90:91], v[54:55], v[2:3] op_sel_hi:[1,0,1]
	v_pk_fma_f32 v[0:1], v[88:89], v[54:55], v[0:1] op_sel_hi:[1,0,1]
	s_and_saveexec_b64 s[38:39], vcc
	s_cbranch_execz .LBB0_27
	v_add_u32_e32 v62, 20, v48
	s_nop 0
	ds_read_b32 v54, v48 offset:32788
	ds_read2st64_b32 v[56:57], v62 offset1:16
	ds_read2st64_b32 v[58:59], v62 offset0:32 offset1:48
	ds_read2st64_b32 v[60:61], v62 offset0:64 offset1:80
	ds_read2st64_b32 v[62:63], v62 offset0:96 offset1:112
	v_add_u32_e32 v55, 3, v49
	s_waitcnt lgkmcnt(3)
	v_mov_b32_e32 v64, v57
	s_waitcnt lgkmcnt(2)
	v_mov_b32_e32 v66, v59
	s_waitcnt lgkmcnt(1)
	v_mov_b32_e32 v68, v61
	s_waitcnt lgkmcnt(0)
	v_mov_b32_e32 v70, v63
	v_cmp_lt_i32_e32 vcc, v55, v43
	s_mov_b64 s[42:43], -1
	s_waitcnt vmcnt(2)
	v_pk_fma_f32 v[34:35], v[94:95], v[56:57], v[34:35] op_sel_hi:[1,0,1]
	v_pk_fma_f32 v[32:33], v[92:93], v[56:57], v[32:33] op_sel_hi:[1,0,1]
	v_pk_fma_f32 v[30:31], v[94:95], v[64:65], v[30:31] op_sel_hi:[1,0,1]
	v_pk_fma_f32 v[28:29], v[92:93], v[64:65], v[28:29] op_sel_hi:[1,0,1]
	v_pk_fma_f32 v[26:27], v[94:95], v[58:59], v[26:27] op_sel_hi:[1,0,1]
	v_pk_fma_f32 v[24:25], v[92:93], v[58:59], v[24:25] op_sel_hi:[1,0,1]
	v_pk_fma_f32 v[22:23], v[94:95], v[66:67], v[22:23] op_sel_hi:[1,0,1]
	v_pk_fma_f32 v[20:21], v[92:93], v[66:67], v[20:21] op_sel_hi:[1,0,1]
	v_pk_fma_f32 v[18:19], v[94:95], v[60:61], v[18:19] op_sel_hi:[1,0,1]
	v_pk_fma_f32 v[16:17], v[92:93], v[60:61], v[16:17] op_sel_hi:[1,0,1]
	v_pk_fma_f32 v[14:15], v[94:95], v[68:69], v[14:15] op_sel_hi:[1,0,1]
	v_pk_fma_f32 v[12:13], v[92:93], v[68:69], v[12:13] op_sel_hi:[1,0,1]
	v_pk_fma_f32 v[10:11], v[94:95], v[62:63], v[10:11] op_sel_hi:[1,0,1]
	v_pk_fma_f32 v[8:9], v[92:93], v[62:63], v[8:9] op_sel_hi:[1,0,1]
	v_pk_fma_f32 v[6:7], v[94:95], v[70:71], v[6:7] op_sel_hi:[1,0,1]
	v_pk_fma_f32 v[4:5], v[92:93], v[70:71], v[4:5] op_sel_hi:[1,0,1]
	v_pk_fma_f32 v[2:3], v[94:95], v[54:55], v[2:3] op_sel_hi:[1,0,1]
	v_pk_fma_f32 v[0:1], v[92:93], v[54:55], v[0:1] op_sel_hi:[1,0,1]
	s_and_saveexec_b64 s[40:41], vcc
	s_cbranch_execz .LBB0_26
	v_add_u32_e32 v62, 24, v48
	s_nop 0
	ds_read_b32 v54, v48 offset:32792
	ds_read2st64_b32 v[56:57], v62 offset1:16
	ds_read2st64_b32 v[58:59], v62 offset0:32 offset1:48
	ds_read2st64_b32 v[60:61], v62 offset0:64 offset1:80
	ds_read2st64_b32 v[62:63], v62 offset0:96 offset1:112
	v_add_u32_e32 v55, 4, v49
	s_waitcnt lgkmcnt(3)
	v_mov_b32_e32 v64, v57
	s_waitcnt lgkmcnt(2)
	v_mov_b32_e32 v66, v59
	s_waitcnt lgkmcnt(1)
	v_mov_b32_e32 v68, v61
	s_waitcnt lgkmcnt(0)
	v_mov_b32_e32 v70, v63
	v_cmp_lt_i32_e32 vcc, v55, v43
	s_mov_b64 s[44:45], -1
	s_waitcnt vmcnt(1)
	v_pk_fma_f32 v[34:35], v[98:99], v[56:57], v[34:35] op_sel_hi:[1,0,1]
	v_pk_fma_f32 v[32:33], v[96:97], v[56:57], v[32:33] op_sel_hi:[1,0,1]
	v_pk_fma_f32 v[30:31], v[98:99], v[64:65], v[30:31] op_sel_hi:[1,0,1]
	v_pk_fma_f32 v[28:29], v[96:97], v[64:65], v[28:29] op_sel_hi:[1,0,1]
	v_pk_fma_f32 v[26:27], v[98:99], v[58:59], v[26:27] op_sel_hi:[1,0,1]
	v_pk_fma_f32 v[24:25], v[96:97], v[58:59], v[24:25] op_sel_hi:[1,0,1]
	v_pk_fma_f32 v[22:23], v[98:99], v[66:67], v[22:23] op_sel_hi:[1,0,1]
	v_pk_fma_f32 v[20:21], v[96:97], v[66:67], v[20:21] op_sel_hi:[1,0,1]
	v_pk_fma_f32 v[18:19], v[98:99], v[60:61], v[18:19] op_sel_hi:[1,0,1]
	v_pk_fma_f32 v[16:17], v[96:97], v[60:61], v[16:17] op_sel_hi:[1,0,1]
	v_pk_fma_f32 v[14:15], v[98:99], v[68:69], v[14:15] op_sel_hi:[1,0,1]
	v_pk_fma_f32 v[12:13], v[96:97], v[68:69], v[12:13] op_sel_hi:[1,0,1]
	v_pk_fma_f32 v[10:11], v[98:99], v[62:63], v[10:11] op_sel_hi:[1,0,1]
	v_pk_fma_f32 v[8:9], v[96:97], v[62:63], v[8:9] op_sel_hi:[1,0,1]
	v_pk_fma_f32 v[6:7], v[98:99], v[70:71], v[6:7] op_sel_hi:[1,0,1]
	v_pk_fma_f32 v[4:5], v[96:97], v[70:71], v[4:5] op_sel_hi:[1,0,1]
	v_pk_fma_f32 v[2:3], v[98:99], v[54:55], v[2:3] op_sel_hi:[1,0,1]
	v_pk_fma_f32 v[0:1], v[96:97], v[54:55], v[0:1] op_sel_hi:[1,0,1]
	s_and_saveexec_b64 s[42:43], vcc
	s_xor_b64 s[42:43], exec, s[42:43]
	s_cbranch_execz .LBB0_25
	v_add_u32_e32 v55, 28, v48
	s_nop 0
	ds_read_b32 v54, v48 offset:32796
	ds_read2st64_b32 v[56:57], v55 offset1:16
	ds_read2st64_b32 v[58:59], v55 offset0:32 offset1:48
	ds_read2st64_b32 v[60:61], v55 offset0:64 offset1:80
	ds_read2st64_b32 v[62:63], v55 offset0:96 offset1:112
	v_add_u32_e32 v65, 8, v49
	v_add_u32_e32 v49, 5, v49
	v_cmp_ge_i32_e32 vcc, v49, v43
	s_waitcnt lgkmcnt(3)
	v_mov_b32_e32 v64, v57
	s_waitcnt lgkmcnt(2)
	v_mov_b32_e32 v66, v59
	s_waitcnt lgkmcnt(1)
	v_mov_b32_e32 v68, v61
	s_waitcnt lgkmcnt(0)
	v_mov_b32_e32 v70, v63
	v_add_u32_e32 v48, 32, v48
	v_lshl_add_u64 v[40:41], v[40:41], 0, s[6:7]
	s_orn2_b64 s[44:45], vcc, exec
	v_mov_b32_e32 v49, v65
	s_waitcnt vmcnt(0)
	v_pk_fma_f32 v[34:35], v[102:103], v[56:57], v[34:35] op_sel_hi:[1,0,1]
	v_pk_fma_f32 v[32:33], v[100:101], v[56:57], v[32:33] op_sel_hi:[1,0,1]
	v_pk_fma_f32 v[30:31], v[102:103], v[64:65], v[30:31] op_sel_hi:[1,0,1]
	v_pk_fma_f32 v[28:29], v[100:101], v[64:65], v[28:29] op_sel_hi:[1,0,1]
	v_pk_fma_f32 v[26:27], v[102:103], v[58:59], v[26:27] op_sel_hi:[1,0,1]
	v_pk_fma_f32 v[24:25], v[100:101], v[58:59], v[24:25] op_sel_hi:[1,0,1]
	v_pk_fma_f32 v[22:23], v[102:103], v[66:67], v[22:23] op_sel_hi:[1,0,1]
	v_pk_fma_f32 v[20:21], v[100:101], v[66:67], v[20:21] op_sel_hi:[1,0,1]
	v_pk_fma_f32 v[18:19], v[102:103], v[60:61], v[18:19] op_sel_hi:[1,0,1]
	v_pk_fma_f32 v[16:17], v[100:101], v[60:61], v[16:17] op_sel_hi:[1,0,1]
	v_pk_fma_f32 v[14:15], v[102:103], v[68:69], v[14:15] op_sel_hi:[1,0,1]
	v_pk_fma_f32 v[12:13], v[100:101], v[68:69], v[12:13] op_sel_hi:[1,0,1]
	v_pk_fma_f32 v[10:11], v[102:103], v[62:63], v[10:11] op_sel_hi:[1,0,1]
	v_pk_fma_f32 v[8:9], v[100:101], v[62:63], v[8:9] op_sel_hi:[1,0,1]
	v_pk_fma_f32 v[6:7], v[102:103], v[70:71], v[6:7] op_sel_hi:[1,0,1]
	v_pk_fma_f32 v[4:5], v[100:101], v[70:71], v[4:5] op_sel_hi:[1,0,1]
	v_pk_fma_f32 v[2:3], v[102:103], v[54:55], v[2:3] op_sel_hi:[1,0,1]
	v_pk_fma_f32 v[0:1], v[100:101], v[54:55], v[0:1] op_sel_hi:[1,0,1]
	s_branch .LBB0_25

.LBB0_167:
	s_or_b64 exec, exec, s[0:1]
	v_readlane_b32 s0, v242, 1
	v_mov_b32_e32 v28, v208
	v_readlane_b32 s1, v242, 2
	s_waitcnt lgkmcnt(0)
	s_barrier
	s_mov_b32 s4, 0
	s_load_dword s2, s[0:1], 0x110
	s_add_u32 s0, s0, 0x110
	s_addc_u32 s1, s1, 0
	v_writelane_b32 v242, s0, 9
	v_ashrrev_i32_e32 v1, 6, v28
	s_waitcnt lgkmcnt(0)
	s_lshl_b32 s71, s2, 3
	s_abs_i32 s6, s71
	v_cvt_f32_u32_e32 v0, s6
	v_writelane_b32 v242, s1, 10
	s_mov_b32 s0, s2
	v_writelane_b32 v242, s0, 11
	v_rcp_iflag_f32_e32 v0, v0
	s_ashr_i32 s2, s71, 31
	v_writelane_b32 v242, s1, 12
	s_add_i32 s0, s71, 0x87ff
	v_mul_f32_e32 v0, 0x4f7ffffe, v0
	v_cvt_u32_f32_e32 v0, v0
	s_ashr_i32 s1, s0, 31
	v_writelane_b32 v242, s2, 13
	s_xor_b32 s1, s1, s2
	s_sub_i32 s2, 0, s6
	v_readfirstlane_b32 s3, v0
	s_mul_i32 s2, s2, s3
	s_mul_hi_u32 s2, s3, s2
	s_abs_i32 s0, s0
	s_add_i32 s2, s3, s2
	v_writelane_b32 v242, s2, 14
	s_mul_hi_u32 s2, s0, s2
	s_mul_i32 s3, s2, s6
	s_sub_i32 s0, s0, s3
	s_add_i32 s3, s2, 1
	s_sub_i32 s5, s0, s6
	s_cmp_ge_u32 s0, s6
	s_cselect_b32 s2, s3, s2
	s_cselect_b32 s0, s5, s0
	s_add_i32 s3, s2, 1
	s_cmp_ge_u32 s0, s6
	s_cselect_b32 s0, s3, s2
	v_writelane_b32 v242, s6, 15
	s_xor_b32 s0, s0, s1
	s_sub_i32 s1, s0, s1
	v_readlane_b32 s0, v242, 0
	s_lshl_b32 s0, s0, 3
	s_nop 0
	v_add_u32_e32 v0, s0, v1
	v_mul_lo_u32 v88, s1, v0
	v_add_u32_e32 v0, s1, v88
	v_min_i32_e32 v90, 0x8800, v0
	v_writelane_b32 v242, s0, 16
	v_cmp_lt_i32_e32 vcc, v88, v90
	v_writelane_b32 v242, s1, 17
	s_and_saveexec_b64 s[0:1], vcc
	s_cbranch_execz .LBB0_174
	v_readlane_b32 s10, v242, 1
	v_readlane_b32 s11, v242, 2
	s_load_dwordx2 s[2:3], s[10:11], s4 offset:0x0
	s_load_dwordx2 s[8:9], s[10:11], s4 offset:0x10
	s_load_dwordx2 s[6:7], s[10:11], s4 offset:0x30
	s_nop 0
	s_load_dwordx2 s[10:11], s[10:11], s4 offset:0x108
	s_mov_b32 s14, 0x8000
	v_add_u32_e32 v16, 0xffff8000, v88
	v_ashrrev_i32_e32 v89, 31, v88
	v_cmp_gt_i32_e32 vcc, s14, v88
	s_waitcnt lgkmcnt(0)
	v_mov_b32_e32 v18, s9
	v_mov_b32_e32 v19, s3
	v_lshlrev_b32_e32 v0, 2, v28
	v_cndmask_b32_e32 v17, 0, v89, vcc
	v_cndmask_b32_e32 v16, v16, v88, vcc
	v_cndmask_b32_e32 v19, v18, v19, vcc
	v_mov_b32_e32 v18, s8
	v_mov_b32_e32 v20, s2
	v_and_b32_e32 v30, 0xfc, v0
	v_cndmask_b32_e32 v18, v18, v20, vcc
	v_lshlrev_b64 v[16:17], 12, v[16:17]
	v_mov_b32_e32 v81, 0
	v_lshlrev_b32_e32 v80, 2, v30
	v_lshl_add_u64 v[16:17], v[18:19], 0, v[16:17]
	v_lshl_add_u64 v[32:33], v[16:17], 0, v[80:81]
	global_load_dwordx4 v[0:3], v80, s[6:7]
	global_load_dwordx4 v[4:7], v80, s[6:7] offset:1024
	global_load_dwordx4 v[8:11], v80, s[6:7] offset:2048
	global_load_dwordx4 v[12:15], v80, s[6:7] offset:3072
	global_load_dwordx4 v[36:39], v[32:33], off
	global_load_dwordx4 v[24:27], v[32:33], off offset:1024
	global_load_dwordx4 v[20:23], v[32:33], off offset:2048
	global_load_dwordx4 v[16:19], v[32:33], off offset:3072
	v_lshl_add_u64 v[32:33], s[10:11], 0, v[80:81]
	s_mov_b64 s[4:5], 0x4000
	v_lshl_add_u64 v[82:83], v[32:33], 0, s[4:5]
	v_lshlrev_b64 v[32:33], 11, v[88:89]
	v_and_b32_e32 v28, 63, v28
	v_lshl_or_b32 v32, v28, 3, v32
	v_lshl_add_u64 v[28:29], s[10:11], 0, v[32:33]
	s_mov_b64 s[4:5], 0xdbff000
	v_lshl_add_u64 v[84:85], v[28:29], 0, s[4:5]
	v_mov_b32_e32 v93, -1
	s_mov_b64 s[10:11], 0
	s_movk_i32 s15, 0x7fff
	v_lshlrev_b32_e32 v80, 2, v30
	v_mov_b32_e32 v91, 0x358637bd
	s_mov_b32 s16, 0xf800000
	v_mov_b32_e32 v92, 0x260
	s_mov_b64 s[12:13], 0x800
	s_waitcnt vmcnt(0)
	s_branch .LBB0_170
